# P1: 80 converter workgroups (176 run the in-projection GEMM)
# baseline (speedup 1.0000x reference)
; #define LAS __attribute__((address_space(3)))
; __device__ __forceinline__ void conv_rest(Frame& F, const Args& a, int gw, int NGW) {
;     LAS unsigned* scr = (LAS unsigned*)(F.lds + F.wave * 13824);
;     bf16_t* Wpa = (bf16_t*)(F.ws + WS_WPA); bf16_t* Wpr = (bf16_t*)(F.ws + WS_WPR); bf16_t* Wout = (bf16_t*)(F.ws + WS_WOUT);
;     unsigned char* Wgu = (unsigned char*)(F.ws + WS_WGU); unsigned char* Wdn = (unsigned char*)(F.ws + WS_WDN);
;     constexpr int I_PA = (GW / 64) * (D / 32), I_PR = (D / 64) * (D / 32), I_OUT = I_PR, I_GU1 = (D / 128) * (4096 / 32), I_DN1 = (DFF / 128) * (D / 32);
;     constexpr int NITEMS = I_PA + I_PR + I_OUT;
;     for (int it = gw; it < NITEMS; it += NGW) {
;         int r = it;
;         if (r < I_PA) { transpose_item(a.in[7], GW, D, Wpa, CM_STD, r, scr, F.lane); continue; } r -= I_PA;
; __global__ void __launch_bounds__(NTHREADS, 2) mk_fwd(Args args) {
;     ...
;         const int nconv = (MK_NCONV * F.G) / 256, ngemm = F.G - nconv;
;         if ((int)blockIdx.x < ngemm) {
;             pg8::DenseSched S; S.init((const bf16_t*)(F.ws + WS_H), D, (const bf16_t*)(F.ws + WS_WIN), D, T, INW, ngemm, (int)blockIdx.x);
;             EpiInProj E{F.ws};
;             if (MK_RSYNC) pg8::gemm_phase<0, EpiInProj, pg8::DenseSched, 127, 127, true>(F.lds, S, E, &bar); else pg8::gemm_phase<0>(F.lds, S, E);
;         } else if (!MK_CONV_IN_P0) conv_rest(F, args, ((int)blockIdx.x - ngemm) * NWAVES + F.wave, nconv * NWAVES);
.LBB0_102:
	s_cmp_lt_i32 s88, 2
	s_cselect_b64 s[4:5], -1, 0
	s_and_b64 s[14:15], s[4:5], s[0:1]
	s_andn2_b64 vcc, exec, s[14:15]
	s_cbranch_vccnz .LBB0_282
	s_ashr_i32 s0, s2, 31
	s_lshr_b32 s0, s0, 30
	s_add_i32 s0, s2, s0
	s_movk_i32 s18, 80
	s_waitcnt vmcnt(6)
	v_mov_b32_e32 v18, v0
	s_sub_i32 s3, s2, s18
	s_cmp_ge_i32 s92, s3
	v_readfirstlane_b32 s4, v18
	s_mov_b64 s[0:1], -1
	s_cbranch_scc0 .LBB0_126
	s_sub_i32 s0, s92, s3
	s_ashr_i32 s19, s4, 6
	s_lshl_b32 s0, s0, 3
	s_add_i32 s21, s19, s0
	s_mul_i32 s0, s19, 0x3600
	s_add_i32 s34, s0, 0
	s_load_dwordx2 s[8:9], s[96:97], 0x68
	s_load_dwordx2 s[0:1], s[96:97], 0x78
	s_waitcnt vmcnt(4)
	v_and_b32_e32 v2, 7, v18
	v_bfe_u32 v1, v18, 3, 3
	v_lshlrev_b32_e32 v164, 4, v2
	s_lshl_b32 s20, s18, 3
	v_lshl_add_u32 v3, v1, 2, s34
	v_mul_u32_u24_e32 v4, 0x210, v2
	v_mul_u32_u24_e32 v5, 0x84, v1
	s_waitcnt vmcnt(2)
	v_add_u32_e32 v6, s34, v164
	v_and_b32_e32 v19, 63, v18
	s_mov_b32 s11, 0
	v_or_b32_e32 v173, 8, v1
	v_or_b32_e32 v168, 16, v1
	v_or_b32_e32 v169, 24, v1
	v_and_b32_e32 v174, 4, v18
	s_cmpk_gt_i32 s21, 0x13ff
	v_add_u32_e32 v170, v3, v4
	v_add_u32_e32 v171, v6, v5
	s_cbranch_scc1 .LBB0_115
	v_mov_b32_e32 v3, 0
	s_load_dwordx4 s[4:7], s[96:97], 0x38
	s_load_dwordx2 s[12:13], s[96:97], 0x48
	v_mov_b32_e32 v165, v3
	v_lshl_add_u64 v[8:9], s[94:95], 0, v[164:165]
	s_mov_b64 s[16:17], 0x3e00000
	v_lshl_add_u64 v[4:5], v[8:9], 0, s[16:17]
	s_mov_b64 s[16:17], 0x3600000
	v_lshlrev_b32_e32 v20, 2, v2
	v_lshlrev_b32_e32 v2, 3, v2
	v_lshl_add_u64 v[6:7], v[8:9], 0, s[16:17]
	s_mov_b64 s[16:17], 0x3200000
	v_lshlrev_b32_e32 v21, 14, v1
	v_and_or_b32 v22, v2, 24, v174
	v_lshlrev_b32_e32 v23, 1, v1
	v_lshl_add_u64 v[8:9], v[8:9], 0, s[16:17]
	v_lshl_or_b32 v24, s21, 6, v2
	s_lshl_b32 s22, s20, 6
	s_lshl_b32 s23, s21, 5
	s_lshl_b32 s24, s20, 5
	s_movk_i32 s25, 0x2000
	s_mov_b32 s26, 0x20000
	s_mov_b32 s27, 0x22000
	s_mov_b32 s28, 0x40000
	s_mov_b32 s29, 0x42000
	s_mov_b32 s30, 0x60000
	s_mov_b32 s31, 0x62000
	v_add_u32_e32 v25, 0x420, v171
	v_add_u32_e32 v26, 0x428, v171
	v_add_u32_e32 v27, 0x840, v171
	v_add_u32_e32 v28, 0x848, v171
	v_add_u32_e32 v29, 0xc60, v171
	s_waitcnt vmcnt(1)
	v_add_u32_e32 v30, 0xc68, v171
	s_mov_b32 s33, s21
	s_branch .LBB0_107
